# MoE down scatter epilogue: slot-table loads hoisted, exec-masked to valid rows (no reads of padding slots), one wait
# baseline (speedup 1.0000x reference)
.LBB0_1070:
	v_lshl_or_b32 v136, s67, 8, v148
	v_ashrrev_i32_e32 v137, 31, v136
	v_add_u32_e32 v192, s49, v138
	v_ashrrev_i32_e32 v193, 31, v192
	v_lshlrev_b64 v[192:193], 2, v[192:193]
	v_lshl_add_u64 v[194:195], s[12:13], 0, v[192:193]
	v_lshl_add_u64 v[192:193], s[8:9], 0, v[192:193]
	v_cmp_gt_i32_e32 vcc, s52, v138
	s_and_saveexec_b64 s[36:37], vcc
	global_load_dword v160, v[192:193], off
	global_load_dword v162, v[194:195], off
	s_or_b64 exec, exec, s[36:37]
	v_add_u32_e32 v196, 16, v138
	v_cmp_gt_i32_e32 vcc, s52, v196
	s_and_saveexec_b64 s[36:37], vcc
	global_load_dword v164, v[192:193], off offset:64
	global_load_dword v166, v[194:195], off offset:64
	s_or_b64 exec, exec, s[36:37]
	v_add_u32_e32 v196, 32, v138
	v_cmp_gt_i32_e32 vcc, s52, v196
	s_and_saveexec_b64 s[36:37], vcc
	global_load_dword v168, v[192:193], off offset:128
	global_load_dword v170, v[194:195], off offset:128
	s_or_b64 exec, exec, s[36:37]
	v_add_u32_e32 v196, 48, v138
	v_cmp_gt_i32_e32 vcc, s52, v196
	s_and_saveexec_b64 s[36:37], vcc
	global_load_dword v172, v[192:193], off offset:192
	global_load_dword v174, v[194:195], off offset:192
	s_or_b64 exec, exec, s[36:37]
	v_add_u32_e32 v196, 128, v138
	v_cmp_gt_i32_e32 vcc, s52, v196
	s_and_saveexec_b64 s[36:37], vcc
	global_load_dword v176, v[192:193], off offset:512
	global_load_dword v178, v[194:195], off offset:512
	s_or_b64 exec, exec, s[36:37]
	v_add_u32_e32 v196, 144, v138
	v_cmp_gt_i32_e32 vcc, s52, v196
	s_and_saveexec_b64 s[36:37], vcc
	global_load_dword v180, v[192:193], off offset:576
	global_load_dword v182, v[194:195], off offset:576
	s_or_b64 exec, exec, s[36:37]
	v_add_u32_e32 v196, 160, v138
	v_cmp_gt_i32_e32 vcc, s52, v196
	s_and_saveexec_b64 s[36:37], vcc
	global_load_dword v184, v[192:193], off offset:640
	global_load_dword v186, v[194:195], off offset:640
	s_or_b64 exec, exec, s[36:37]
	v_add_u32_e32 v196, 176, v138
	v_cmp_gt_i32_e32 vcc, s52, v196
	s_and_saveexec_b64 s[36:37], vcc
	global_load_dword v188, v[192:193], off offset:704
	global_load_dword v190, v[194:195], off offset:704
	s_or_b64 exec, exec, s[36:37]
	s_waitcnt vmcnt(0)
	v_cmp_gt_i32_e32 vcc, s52, v138
	s_and_saveexec_b64 s[36:37], vcc
	s_cbranch_execz .LBB0_1072
	v_mov_b32_e32 v152, 0
	v_mov_b32_e32 v153, 0
	v_mov_b32_e32 v154, 0
	v_mov_b32_e32 v155, 0
	v_ashrrev_i32_e32 v161, 31, v160
	v_mul_f32_e32 v162, 0x41800000, v162
	v_pk_mul_f32 v[112:113], v[112:113], v[162:163] op_sel_hi:[1,0]
	v_pk_mul_f32 v[116:117], v[116:117], v[162:163] op_sel_hi:[1,0]
	v_pk_mul_f32 v[120:121], v[120:121], v[162:163] op_sel_hi:[1,0]
	v_pk_mul_f32 v[124:125], v[124:125], v[162:163] op_sel_hi:[1,0]
	v_cvt_pk_fp8_f32 v152, v112, v113
	v_cvt_pk_fp8_f32 v153, v116, v117
	v_cvt_pk_fp8_f32 v154, v120, v121
	v_cvt_pk_fp8_f32 v155, v124, v125
	v_pk_mul_f32 v[114:115], v[114:115], v[162:163] op_sel_hi:[1,0]
	v_pk_mul_f32 v[118:119], v[118:119], v[162:163] op_sel_hi:[1,0]
	v_pk_mul_f32 v[122:123], v[122:123], v[162:163] op_sel_hi:[1,0]
	v_pk_mul_f32 v[126:127], v[126:127], v[162:163] op_sel_hi:[1,0]
	v_cvt_pk_fp8_f32 v152, v114, v115 op_sel:[0,0,1]
	v_cvt_pk_fp8_f32 v153, v118, v119 op_sel:[0,0,1]
	v_cvt_pk_fp8_f32 v154, v122, v123 op_sel:[0,0,1]
	v_cvt_pk_fp8_f32 v155, v126, v127 op_sel:[0,0,1]
	v_lshlrev_b64 v[112:113], 10, v[160:161]
	v_lshl_add_u64 v[112:113], s[6:7], 0, v[112:113]
	v_lshl_add_u64 v[112:113], v[112:113], 0, v[136:137]
	global_store_dwordx4 v[112:113], v[152:155], off

.LBB0_4461:
	v_lshl_or_b32 v136, s66, 8, v148
	v_ashrrev_i32_e32 v137, 31, v136
	v_add_u32_e32 v192, s48, v138
	v_ashrrev_i32_e32 v193, 31, v192
	v_lshlrev_b64 v[192:193], 2, v[192:193]
	v_lshl_add_u64 v[194:195], s[12:13], 0, v[192:193]
	v_lshl_add_u64 v[192:193], s[8:9], 0, v[192:193]
	v_cmp_gt_i32_e32 vcc, s51, v138
	s_and_saveexec_b64 s[36:37], vcc
	global_load_dword v160, v[192:193], off
	global_load_dword v162, v[194:195], off
	s_or_b64 exec, exec, s[36:37]
	v_add_u32_e32 v196, 16, v138
	v_cmp_gt_i32_e32 vcc, s51, v196
	s_and_saveexec_b64 s[36:37], vcc
	global_load_dword v164, v[192:193], off offset:64
	global_load_dword v166, v[194:195], off offset:64
	s_or_b64 exec, exec, s[36:37]
	v_add_u32_e32 v196, 32, v138
	v_cmp_gt_i32_e32 vcc, s51, v196
	s_and_saveexec_b64 s[36:37], vcc
	global_load_dword v168, v[192:193], off offset:128
	global_load_dword v170, v[194:195], off offset:128
	s_or_b64 exec, exec, s[36:37]
	v_add_u32_e32 v196, 48, v138
	v_cmp_gt_i32_e32 vcc, s51, v196
	s_and_saveexec_b64 s[36:37], vcc
	global_load_dword v172, v[192:193], off offset:192
	global_load_dword v174, v[194:195], off offset:192
	s_or_b64 exec, exec, s[36:37]
	v_add_u32_e32 v196, 128, v138
	v_cmp_gt_i32_e32 vcc, s51, v196
	s_and_saveexec_b64 s[36:37], vcc
	global_load_dword v176, v[192:193], off offset:512
	global_load_dword v178, v[194:195], off offset:512
	s_or_b64 exec, exec, s[36:37]
	v_add_u32_e32 v196, 144, v138
	v_cmp_gt_i32_e32 vcc, s51, v196
	s_and_saveexec_b64 s[36:37], vcc
	global_load_dword v180, v[192:193], off offset:576
	global_load_dword v182, v[194:195], off offset:576
	s_or_b64 exec, exec, s[36:37]
	v_add_u32_e32 v196, 160, v138
	v_cmp_gt_i32_e32 vcc, s51, v196
	s_and_saveexec_b64 s[36:37], vcc
	global_load_dword v184, v[192:193], off offset:640
	global_load_dword v186, v[194:195], off offset:640
	s_or_b64 exec, exec, s[36:37]
	v_add_u32_e32 v196, 176, v138
	v_cmp_gt_i32_e32 vcc, s51, v196
	s_and_saveexec_b64 s[36:37], vcc
	global_load_dword v188, v[192:193], off offset:704
	global_load_dword v190, v[194:195], off offset:704
	s_or_b64 exec, exec, s[36:37]
	s_waitcnt vmcnt(0)
	v_cmp_gt_i32_e32 vcc, s51, v138
	s_and_saveexec_b64 s[36:37], vcc
	s_cbranch_execz .LBB0_4463
	v_mov_b32_e32 v152, 0
	v_mov_b32_e32 v153, 0
	v_mov_b32_e32 v154, 0
	v_mov_b32_e32 v155, 0
	v_ashrrev_i32_e32 v161, 31, v160
	v_mul_f32_e32 v162, 0x41800000, v162
	v_pk_mul_f32 v[112:113], v[112:113], v[162:163] op_sel_hi:[1,0]
	v_pk_mul_f32 v[116:117], v[116:117], v[162:163] op_sel_hi:[1,0]
	v_pk_mul_f32 v[120:121], v[120:121], v[162:163] op_sel_hi:[1,0]
	v_pk_mul_f32 v[124:125], v[124:125], v[162:163] op_sel_hi:[1,0]
	v_cvt_pk_fp8_f32 v152, v112, v113
	v_cvt_pk_fp8_f32 v153, v116, v117
	v_cvt_pk_fp8_f32 v154, v120, v121
	v_cvt_pk_fp8_f32 v155, v124, v125
	v_pk_mul_f32 v[114:115], v[114:115], v[162:163] op_sel_hi:[1,0]
	v_pk_mul_f32 v[118:119], v[118:119], v[162:163] op_sel_hi:[1,0]
	v_pk_mul_f32 v[122:123], v[122:123], v[162:163] op_sel_hi:[1,0]
	v_pk_mul_f32 v[126:127], v[126:127], v[162:163] op_sel_hi:[1,0]
	v_cvt_pk_fp8_f32 v152, v114, v115 op_sel:[0,0,1]
	v_cvt_pk_fp8_f32 v153, v118, v119 op_sel:[0,0,1]
	v_cvt_pk_fp8_f32 v154, v122, v123 op_sel:[0,0,1]
	v_cvt_pk_fp8_f32 v155, v126, v127 op_sel:[0,0,1]
	v_lshlrev_b64 v[112:113], 10, v[160:161]
	v_lshl_add_u64 v[112:113], s[6:7], 0, v[112:113]
	v_lshl_add_u64 v[112:113], v[112:113], 0, v[136:137]
	global_store_dwordx4 v[112:113], v[152:155], off
